# pool_main: both per-column scale loads requested at the start of pool_main into free registers (they were issued right before use and waited with vmcnt(0))
# speedup vs baseline: 1.0094x; 1.0094x over previous
.LBB0_597:
	v_sub_f32_e32 v2, v137, v2
	v_cvt_pk_bf16_f32 v2, v2, s0
	s_mov_b64 s[4:5], s[0:1]
	ds_write_b16 v0, v2 offset:65520
	s_waitcnt lgkmcnt(0)
	s_barrier
	s_load_dwordx2 s[8:9], s[4:5], 0xd0
	s_nop 0
	s_load_dwordx2 s[4:5], s[4:5], 0x68
	v_mbcnt_lo_u32_b32 v0, -1, 0
	v_mbcnt_hi_u32_b32 v0, -1, v0
	s_add_i32 s34, s34, s46
	v_add_u32_e32 v0, s67, v0
	s_waitcnt lgkmcnt(0)
	s_add_u32 s6, s4, s38
	v_readfirstlane_b32 s4, v0
	s_addc_u32 s7, s5, s39
	v_and_b32_e32 v164, 31, v234
	v_or_b32_e32 v164, s67, v164
	v_ashrrev_i32_e32 v165, 31, v164
	v_lshl_add_u64 v[164:165], v[164:165], 2, s[6:7]
	global_load_dword v166, v[164:165], off
	global_load_dword v167, v[164:165], off offset:128
	s_ashr_i32 s10, s4, 7
	s_ashr_i32 s11, s10, 31
	s_and_b32 s5, s4, 64
	s_lshl_b64 s[10:11], s[10:11], 7
	v_and_b32_e32 v123, 31, v0
	s_or_b32 s5, s10, s5
	v_or_b32_e32 v2, s5, v123
	v_mov_b32_e32 v3, s11
	v_bfe_u32 v122, v0, 5, 1
	v_lshlrev_b64 v[2:3], 8, v[2:3]
	v_lshl_add_u64 v[2:3], s[8:9], 0, v[2:3]
	v_lshlrev_b32_e32 v0, 4, v122
	v_lshl_add_u64 v[6:7], v[2:3], 0, v[0:1]
	s_mov_b32 s5, 0x1600000
	v_add_co_u32_e32 v2, vcc, s5, v6
	s_mov_b64 s[8:9], 0x1600000
	s_nop 0
	v_addc_co_u32_e32 v3, vcc, 0, v7, vcc
	global_load_dwordx4 v[2:5], v[2:3], off
	v_lshl_add_u64 v[114:115], v[6:7], 0, s[8:9]
	s_mov_b64 s[8:9], 0x1602000
	s_mov_b32 s5, 0x1602000
	v_lshl_add_u64 v[156:157], v[6:7], 0, s[8:9]
	v_add_co_u32_e32 v6, vcc, s5, v6
	s_lshl_b32 s5, s4, 1
	s_nop 0
	v_addc_co_u32_e32 v7, vcc, 0, v7, vcc
	global_load_dwordx4 v[6:9], v[6:7], off
	s_nop 0
	global_load_dwordx4 v[124:127], v[114:115], off offset:32
	global_load_dwordx4 v[128:131], v[156:157], off offset:32
	global_load_dwordx4 v[132:135], v[114:115], off offset:64
	global_load_dwordx4 v[136:139], v[156:157], off offset:64
	global_load_dwordx4 v[140:143], v[114:115], off offset:96
	global_load_dwordx4 v[144:147], v[156:157], off offset:96
	s_and_b32 s5, s5, 0xffffff00
	v_mul_u32_u24_e32 v10, 0x410, v123
	v_or_b32_e32 v0, s5, v0
	v_add3_u32 v0, 0, v10, v0
	ds_read_b128 v[10:13], v0 offset:33280
	ds_read_b128 v[14:17], v0
	ds_read_b128 v[148:151], v0 offset:32
	ds_read_b128 v[152:155], v0 offset:33312
	s_andn2_b32 s4, s4, 63
	v_mul_u32_u24_e32 v122, 0x1040, v122
	s_cmpk_gt_i32 s34, 0x1ff
	s_waitcnt vmcnt(6) lgkmcnt(2)
	v_mfma_f32_32x32x16_bf16 v[18:33], v[14:17], v[6:9], 0
	v_mfma_f32_32x32x16_bf16 v[50:65], v[14:17], v[2:5], 0
	v_mfma_f32_32x32x16_bf16 v[34:49], v[10:13], v[2:5], 0
	v_mfma_f32_32x32x16_bf16 v[2:17], v[10:13], v[6:9], 0
	s_waitcnt vmcnt(5) lgkmcnt(1)
	v_mfma_f32_32x32x16_bf16 v[50:65], v[148:151], v[124:127], v[50:65]
	s_waitcnt vmcnt(4)
	v_mfma_f32_32x32x16_bf16 v[18:33], v[148:151], v[128:131], v[18:33]
	s_waitcnt lgkmcnt(0)
	v_mfma_f32_32x32x16_bf16 v[34:49], v[152:155], v[124:127], v[34:49]
	v_mfma_f32_32x32x16_bf16 v[2:17], v[152:155], v[128:131], v[2:17]
	ds_read_b128 v[124:127], v0 offset:64
	ds_read_b128 v[128:131], v0 offset:33344
	s_waitcnt vmcnt(3) lgkmcnt(1)
	v_mfma_f32_32x32x16_bf16 v[50:65], v[124:127], v[132:135], v[50:65]
	s_waitcnt vmcnt(2)
	v_mfma_f32_32x32x16_bf16 v[18:33], v[124:127], v[136:139], v[18:33]
	s_waitcnt lgkmcnt(0)
	v_mfma_f32_32x32x16_bf16 v[34:49], v[128:131], v[132:135], v[34:49]
	v_mfma_f32_32x32x16_bf16 v[2:17], v[128:131], v[136:139], v[2:17]
	ds_read_b128 v[124:127], v0 offset:96
	ds_read_b128 v[128:131], v0 offset:33376
	s_waitcnt vmcnt(1) lgkmcnt(1)
	v_mfma_f32_32x32x16_bf16 v[50:65], v[124:127], v[140:143], v[50:65]
	s_waitcnt vmcnt(0)
	v_mfma_f32_32x32x16_bf16 v[18:33], v[124:127], v[144:147], v[18:33]
	s_waitcnt lgkmcnt(0)
	v_mfma_f32_32x32x16_bf16 v[34:49], v[128:131], v[140:143], v[34:49]
	v_mfma_f32_32x32x16_bf16 v[2:17], v[128:131], v[144:147], v[2:17]
	global_load_dwordx4 v[124:127], v[114:115], off offset:128
	global_load_dwordx4 v[128:131], v[156:157], off offset:128
	global_load_dwordx4 v[132:135], v[114:115], off offset:160
	global_load_dwordx4 v[136:139], v[156:157], off offset:160
	global_load_dwordx4 v[140:143], v[114:115], off offset:192
	global_load_dwordx4 v[144:147], v[156:157], off offset:192
	global_load_dwordx4 v[148:151], v[114:115], off offset:224
	global_load_dwordx4 v[152:155], v[156:157], off offset:224
	ds_read_b128 v[156:159], v0 offset:128
	ds_read_b128 v[160:163], v0 offset:33408
	s_waitcnt vmcnt(7) lgkmcnt(1)
	v_mfma_f32_32x32x16_bf16 v[50:65], v[156:159], v[124:127], v[50:65]
	s_waitcnt vmcnt(6)
	v_mfma_f32_32x32x16_bf16 v[18:33], v[156:159], v[128:131], v[18:33]
	s_waitcnt lgkmcnt(0)
	v_mfma_f32_32x32x16_bf16 v[34:49], v[160:163], v[124:127], v[34:49]
	v_mfma_f32_32x32x16_bf16 v[2:17], v[160:163], v[128:131], v[2:17]
	ds_read_b128 v[124:127], v0 offset:160
	ds_read_b128 v[128:131], v0 offset:33440
	s_waitcnt vmcnt(5) lgkmcnt(1)
	v_mfma_f32_32x32x16_bf16 v[50:65], v[124:127], v[132:135], v[50:65]
	s_waitcnt vmcnt(4)
	v_mfma_f32_32x32x16_bf16 v[18:33], v[124:127], v[136:139], v[18:33]
	s_waitcnt lgkmcnt(0)
	v_mfma_f32_32x32x16_bf16 v[34:49], v[128:131], v[132:135], v[34:49]
	v_mfma_f32_32x32x16_bf16 v[2:17], v[128:131], v[136:139], v[2:17]
	ds_read_b128 v[124:127], v0 offset:192
	ds_read_b128 v[128:131], v0 offset:33472
	s_waitcnt vmcnt(3) lgkmcnt(1)
	v_mfma_f32_32x32x16_bf16 v[50:65], v[124:127], v[140:143], v[50:65]
	s_waitcnt vmcnt(2)
	v_mfma_f32_32x32x16_bf16 v[18:33], v[124:127], v[144:147], v[18:33]
	s_waitcnt lgkmcnt(0)
	v_mfma_f32_32x32x16_bf16 v[34:49], v[128:131], v[140:143], v[34:49]
	v_mfma_f32_32x32x16_bf16 v[2:17], v[128:131], v[144:147], v[2:17]
	ds_read_b128 v[124:127], v0 offset:224
	ds_read_b128 v[128:131], v0 offset:33504
	s_waitcnt lgkmcnt(0)
	s_barrier
	s_waitcnt vmcnt(1)
	v_mfma_f32_32x32x16_bf16 v[50:65], v[124:127], v[148:151], v[50:65]
	s_waitcnt vmcnt(0)
	v_mfma_f32_32x32x16_bf16 v[18:33], v[124:127], v[152:155], v[18:33]
	v_or_b32_e32 v124, s4, v123
	v_ashrrev_i32_e32 v125, 31, v124
	v_lshl_add_u64 v[114:115], v[124:125], 2, s[6:7]
	v_mov_b32_e32 v123, v166
	v_lshlrev_b32_e32 v0, 1, v124
	v_add3_u32 v0, 0, v0, v122
	s_waitcnt vmcnt(0)
	s_nop 2
	v_mul_f32_e32 v50, v50, v123
	v_mfma_f32_32x32x16_bf16 v[34:49], v[128:131], v[148:151], v[34:49]
	v_cvt_pk_bf16_f32 v50, v50, s0
	ds_write_b16 v0, v50
	v_mul_f32_e32 v50, v51, v123
	v_cvt_pk_bf16_f32 v50, v50, s0
	ds_write_b16 v0, v50 offset:1040
	v_mul_f32_e32 v50, v52, v123
	v_cvt_pk_bf16_f32 v50, v50, s0
	s_nop 4
	v_mul_f32_e32 v34, v34, v123
	v_cvt_pk_bf16_f32 v34, v34, s0
	ds_write_b16 v0, v34 offset:33280
	v_mul_f32_e32 v34, v35, v123
	v_cvt_pk_bf16_f32 v34, v34, s0
	ds_write_b16 v0, v34 offset:34320
	v_mul_f32_e32 v34, v36, v123
	v_cvt_pk_bf16_f32 v34, v34, s0
	ds_write_b16 v0, v34 offset:35360
	v_mul_f32_e32 v34, v37, v123
	v_cvt_pk_bf16_f32 v34, v34, s0
	ds_write_b16 v0, v34 offset:36400
	v_mul_f32_e32 v34, v38, v123
	v_cvt_pk_bf16_f32 v34, v34, s0
	ds_write_b16 v0, v34 offset:41600
	v_mul_f32_e32 v34, v39, v123
	v_cvt_pk_bf16_f32 v34, v34, s0
	ds_write_b16 v0, v34 offset:42640
	v_mul_f32_e32 v34, v40, v123
	v_cvt_pk_bf16_f32 v34, v34, s0
	ds_write_b16 v0, v34 offset:43680
	v_mul_f32_e32 v34, v41, v123
	v_cvt_pk_bf16_f32 v34, v34, s0
	ds_write_b16 v0, v34 offset:44720
	v_mul_f32_e32 v34, v42, v123
	v_cvt_pk_bf16_f32 v34, v34, s0
	ds_write_b16 v0, v34 offset:49920
	v_mul_f32_e32 v34, v43, v123
	v_cvt_pk_bf16_f32 v34, v34, s0
	ds_write_b16 v0, v34 offset:50960
	v_mul_f32_e32 v34, v44, v123
	v_cvt_pk_bf16_f32 v34, v34, s0
	ds_write_b16 v0, v34 offset:52000
	v_mul_f32_e32 v34, v45, v123
	v_cvt_pk_bf16_f32 v34, v34, s0
	ds_write_b16 v0, v34 offset:53040
	v_mul_f32_e32 v34, v46, v123
	v_cvt_pk_bf16_f32 v34, v34, s0
	ds_write_b16 v0, v34 offset:58240
	v_mul_f32_e32 v34, v47, v123
	v_cvt_pk_bf16_f32 v34, v34, s0
	ds_write_b16 v0, v34 offset:59280
	v_mul_f32_e32 v34, v48, v123
	v_cvt_pk_bf16_f32 v34, v34, s0
	ds_write_b16 v0, v34 offset:60320
	v_mul_f32_e32 v34, v49, v123
	v_cvt_pk_bf16_f32 v34, v34, s0
	ds_write_b16 v0, v34 offset:61360
	v_mov_b32_e32 v34, v167
	v_mfma_f32_32x32x16_bf16 v[2:17], v[128:131], v[152:155], v[2:17]
	ds_write_b16 v0, v50 offset:2080
	v_mul_f32_e32 v50, v53, v123
	v_cvt_pk_bf16_f32 v50, v50, s0
	ds_write_b16 v0, v50 offset:3120
	v_mul_f32_e32 v50, v54, v123
	v_cvt_pk_bf16_f32 v50, v50, s0
	ds_write_b16 v0, v50 offset:8320
	v_mul_f32_e32 v50, v55, v123
	v_cvt_pk_bf16_f32 v50, v50, s0
	ds_write_b16 v0, v50 offset:9360
	v_mul_f32_e32 v50, v56, v123
	v_cvt_pk_bf16_f32 v50, v50, s0
	ds_write_b16 v0, v50 offset:10400
	v_mul_f32_e32 v50, v57, v123
	v_cvt_pk_bf16_f32 v50, v50, s0
	ds_write_b16 v0, v50 offset:11440
	v_mul_f32_e32 v50, v58, v123
	v_cvt_pk_bf16_f32 v50, v50, s0
	ds_write_b16 v0, v50 offset:16640
	v_mul_f32_e32 v50, v59, v123
	v_cvt_pk_bf16_f32 v50, v50, s0
	ds_write_b16 v0, v50 offset:17680
	v_mul_f32_e32 v50, v60, v123
	v_cvt_pk_bf16_f32 v50, v50, s0
	ds_write_b16 v0, v50 offset:18720
	v_mul_f32_e32 v50, v61, v123
	v_cvt_pk_bf16_f32 v50, v50, s0
	ds_write_b16 v0, v50 offset:19760
	v_mul_f32_e32 v50, v62, v123
	v_cvt_pk_bf16_f32 v50, v50, s0
	ds_write_b16 v0, v50 offset:24960
	v_mul_f32_e32 v50, v63, v123
	v_cvt_pk_bf16_f32 v50, v50, s0
	ds_write_b16 v0, v50 offset:26000
	v_mul_f32_e32 v50, v64, v123
	v_cvt_pk_bf16_f32 v50, v50, s0
	ds_write_b16 v0, v50 offset:27040
	v_mul_f32_e32 v50, v65, v123
	v_cvt_pk_bf16_f32 v50, v50, s0
	ds_write_b16 v0, v50 offset:28080
	s_waitcnt vmcnt(0)
	v_mul_f32_e32 v18, v18, v34
	v_mul_f32_e32 v2, v2, v34
	v_cvt_pk_bf16_f32 v18, v18, s0
	v_cvt_pk_bf16_f32 v2, v2, s0
	ds_write_b16 v0, v18 offset:64
	v_mul_f32_e32 v18, v19, v34
	ds_write_b16 v0, v2 offset:33344
	v_mul_f32_e32 v2, v3, v34
	v_cvt_pk_bf16_f32 v18, v18, s0
	v_cvt_pk_bf16_f32 v2, v2, s0
	ds_write_b16 v0, v18 offset:1104
	v_mul_f32_e32 v18, v20, v34
	ds_write_b16 v0, v2 offset:34384
	v_mul_f32_e32 v2, v4, v34
	v_cvt_pk_bf16_f32 v18, v18, s0
	v_cvt_pk_bf16_f32 v2, v2, s0
	ds_write_b16 v0, v18 offset:2144
	v_mul_f32_e32 v18, v21, v34
	ds_write_b16 v0, v2 offset:35424
	v_mul_f32_e32 v2, v5, v34
	v_cvt_pk_bf16_f32 v18, v18, s0
	v_cvt_pk_bf16_f32 v2, v2, s0
	ds_write_b16 v0, v18 offset:3184
	v_mul_f32_e32 v18, v22, v34
	ds_write_b16 v0, v2 offset:36464
	v_mul_f32_e32 v2, v6, v34
	v_cvt_pk_bf16_f32 v18, v18, s0
	v_cvt_pk_bf16_f32 v2, v2, s0
	ds_write_b16 v0, v18 offset:8384
	v_mul_f32_e32 v18, v23, v34
	ds_write_b16 v0, v2 offset:41664
	v_mul_f32_e32 v2, v7, v34
	v_cvt_pk_bf16_f32 v18, v18, s0
	v_cvt_pk_bf16_f32 v2, v2, s0
	ds_write_b16 v0, v18 offset:9424
	v_mul_f32_e32 v18, v24, v34
	ds_write_b16 v0, v2 offset:42704
	v_mul_f32_e32 v2, v8, v34
	v_cvt_pk_bf16_f32 v18, v18, s0
	v_cvt_pk_bf16_f32 v2, v2, s0
	ds_write_b16 v0, v18 offset:10464
	v_mul_f32_e32 v18, v25, v34
	ds_write_b16 v0, v2 offset:43744
	v_mul_f32_e32 v2, v9, v34
	v_cvt_pk_bf16_f32 v18, v18, s0
	v_cvt_pk_bf16_f32 v2, v2, s0
	ds_write_b16 v0, v18 offset:11504
	v_mul_f32_e32 v18, v26, v34
	ds_write_b16 v0, v2 offset:44784
	v_mul_f32_e32 v2, v10, v34
	v_cvt_pk_bf16_f32 v18, v18, s0
	v_cvt_pk_bf16_f32 v2, v2, s0
	ds_write_b16 v0, v18 offset:16704
	v_mul_f32_e32 v18, v27, v34
	ds_write_b16 v0, v2 offset:49984
	v_mul_f32_e32 v2, v11, v34
	v_cvt_pk_bf16_f32 v18, v18, s0
	v_cvt_pk_bf16_f32 v2, v2, s0
	ds_write_b16 v0, v18 offset:17744
	v_mul_f32_e32 v18, v28, v34
	ds_write_b16 v0, v2 offset:51024
	v_mul_f32_e32 v2, v12, v34
	v_cvt_pk_bf16_f32 v18, v18, s0
	v_cvt_pk_bf16_f32 v2, v2, s0
	ds_write_b16 v0, v18 offset:18784
	v_mul_f32_e32 v18, v29, v34
	ds_write_b16 v0, v2 offset:52064
	v_mul_f32_e32 v2, v13, v34
	v_cvt_pk_bf16_f32 v18, v18, s0
	v_cvt_pk_bf16_f32 v2, v2, s0
	ds_write_b16 v0, v18 offset:19824
	v_mul_f32_e32 v18, v30, v34
	ds_write_b16 v0, v2 offset:53104
	v_mul_f32_e32 v2, v14, v34
	v_cvt_pk_bf16_f32 v18, v18, s0
	v_cvt_pk_bf16_f32 v2, v2, s0
	ds_write_b16 v0, v18 offset:25024
	v_mul_f32_e32 v18, v31, v34
	ds_write_b16 v0, v2 offset:58304
	v_mul_f32_e32 v2, v15, v34
	v_cvt_pk_bf16_f32 v18, v18, s0
	v_cvt_pk_bf16_f32 v2, v2, s0
	ds_write_b16 v0, v18 offset:26064
	v_mul_f32_e32 v18, v32, v34
	ds_write_b16 v0, v2 offset:59344
	v_mul_f32_e32 v2, v16, v34
	v_cvt_pk_bf16_f32 v18, v18, s0
	v_cvt_pk_bf16_f32 v2, v2, s0
	ds_write_b16 v0, v18 offset:27104
	v_mul_f32_e32 v18, v33, v34
	ds_write_b16 v0, v2 offset:60384
	v_mul_f32_e32 v2, v17, v34
	v_cvt_pk_bf16_f32 v18, v18, s0
	v_cvt_pk_bf16_f32 v2, v2, s0
	ds_write_b16 v0, v18 offset:28144
	ds_write_b16 v0, v2 offset:61424
	s_waitcnt lgkmcnt(0)
	s_barrier
	s_cbranch_scc1 .LBB0_599
	s_mov_b64 s[4:5], s[0:1]
	s_load_dwordx2 s[4:5], s[4:5], 0xd0
	s_bfe_i32 s9, s34, 0x10019
	v_mbcnt_lo_u32_b32 v0, -1, 0
	v_mbcnt_hi_u32_b32 v0, -1, v0
	s_lshl_b32 s8, s34, 6
	v_add_u32_e32 v8, s67, v0
	s_lshr_b32 s9, s9, 21
	s_add_i32 s9, s8, s9
	v_lshlrev_b32_e32 v0, 4, v8
	s_and_b32 s9, s9, 0xfffff800
	v_and_b32_e32 v0, 0x3f0, v0
	s_sub_i32 s8, s9, s8
	s_waitcnt lgkmcnt(0)
	v_lshl_add_u64 v[2:3], s[4:5], 0, v[0:1]
	v_min_i32_e32 v0, 0x177f, v8
	s_or_b32 s8, s8, 30
	v_ashrrev_i32_e32 v0, 6, v0
	s_ashr_i32 s35, s34, 31
	v_max_i32_e32 v4, s8, v0
	v_min_i32_e32 v0, 0x157f, v8
	s_lshl_b64 s[6:7], s[34:35], 6
	v_add_u32_e32 v0, 0x200, v0
	s_add_u32 s6, s6, 0xffffffe2
	v_ashrrev_i32_e32 v0, 6, v0
	s_addc_u32 s7, s7, -1
	v_ashrrev_i32_e32 v5, 31, v4
	v_max_i32_e32 v6, s8, v0
	s_mov_b64 s[4:5], 0xfc00000
	v_lshl_add_u64 v[4:5], s[6:7], 0, v[4:5]
	v_ashrrev_i32_e32 v7, 31, v6
	v_min_i32_e32 v0, 0x137f, v8
	v_lshl_add_u64 v[2:3], v[2:3], 0, s[4:5]
	v_lshlrev_b64 v[4:5], 10, v[4:5]
	v_lshl_add_u64 v[6:7], s[6:7], 0, v[6:7]
	v_add_u32_e32 v0, 0x400, v0
	v_lshl_add_u64 v[4:5], v[2:3], 0, v[4:5]
	v_lshlrev_b64 v[6:7], 10, v[6:7]
	v_ashrrev_i32_e32 v0, 6, v0
	v_lshl_add_u64 v[6:7], v[2:3], 0, v[6:7]
	global_load_dwordx4 v[66:69], v[4:5], off
	global_load_dwordx4 v[70:73], v[6:7], off
	v_max_i32_e32 v4, s8, v0
	v_min_i32_e32 v0, 0x117f, v8
	v_add_u32_e32 v0, 0x600, v0
	v_ashrrev_i32_e32 v0, 6, v0
	v_ashrrev_i32_e32 v5, 31, v4
	v_max_i32_e32 v6, s8, v0
	v_lshl_add_u64 v[4:5], s[6:7], 0, v[4:5]
	v_ashrrev_i32_e32 v7, 31, v6
	v_min_i32_e32 v0, 0xf7f, v8
	v_lshlrev_b64 v[4:5], 10, v[4:5]
	v_lshl_add_u64 v[6:7], s[6:7], 0, v[6:7]
	v_add_u32_e32 v0, 0x800, v0
	v_lshl_add_u64 v[4:5], v[2:3], 0, v[4:5]
	v_lshlrev_b64 v[6:7], 10, v[6:7]
	v_ashrrev_i32_e32 v0, 6, v0
	v_lshl_add_u64 v[6:7], v[2:3], 0, v[6:7]
	global_load_dwordx4 v[74:77], v[4:5], off
	global_load_dwordx4 v[78:81], v[6:7], off
	v_max_i32_e32 v4, s8, v0
	v_min_i32_e32 v0, 0xd7f, v8
	v_add_u32_e32 v0, 0xa00, v0
	v_ashrrev_i32_e32 v0, 6, v0
	v_ashrrev_i32_e32 v5, 31, v4
	v_max_i32_e32 v6, s8, v0
	v_lshl_add_u64 v[4:5], s[6:7], 0, v[4:5]
	v_ashrrev_i32_e32 v7, 31, v6
	v_min_i32_e32 v0, 0xb7f, v8
	v_lshlrev_b64 v[4:5], 10, v[4:5]
	v_lshl_add_u64 v[6:7], s[6:7], 0, v[6:7]
	v_add_u32_e32 v0, 0xc00, v0
	v_lshl_add_u64 v[4:5], v[2:3], 0, v[4:5]
	v_lshlrev_b64 v[6:7], 10, v[6:7]
	v_ashrrev_i32_e32 v0, 6, v0
	v_lshl_add_u64 v[6:7], v[2:3], 0, v[6:7]
	global_load_dwordx4 v[82:85], v[4:5], off
	global_load_dwordx4 v[86:89], v[6:7], off
	v_max_i32_e32 v4, s8, v0
	v_min_i32_e32 v0, 0x97f, v8
	v_add_u32_e32 v0, 0xe00, v0
	v_ashrrev_i32_e32 v0, 6, v0
	v_ashrrev_i32_e32 v5, 31, v4
	v_max_i32_e32 v6, s8, v0
	v_lshl_add_u64 v[4:5], s[6:7], 0, v[4:5]
	v_ashrrev_i32_e32 v7, 31, v6
	v_min_i32_e32 v0, 0x77f, v8
	v_lshlrev_b64 v[4:5], 10, v[4:5]
	v_lshl_add_u64 v[6:7], s[6:7], 0, v[6:7]
	v_add_u32_e32 v0, 0x1000, v0
	v_lshl_add_u64 v[4:5], v[2:3], 0, v[4:5]
	v_lshlrev_b64 v[6:7], 10, v[6:7]
	v_ashrrev_i32_e32 v0, 6, v0
	v_lshl_add_u64 v[6:7], v[2:3], 0, v[6:7]
	global_load_dwordx4 v[90:93], v[4:5], off
	global_load_dwordx4 v[94:97], v[6:7], off
	v_max_i32_e32 v4, s8, v0
	v_min_i32_e32 v0, 0x57f, v8
	v_add_u32_e32 v0, 0x1200, v0
	v_ashrrev_i32_e32 v0, 6, v0
	v_ashrrev_i32_e32 v5, 31, v4
	v_max_i32_e32 v6, s8, v0
	v_lshl_add_u64 v[4:5], s[6:7], 0, v[4:5]
	v_ashrrev_i32_e32 v7, 31, v6
	v_min_i32_e32 v0, 0x37f, v8
	v_lshlrev_b64 v[4:5], 10, v[4:5]
	v_lshl_add_u64 v[6:7], s[6:7], 0, v[6:7]
	v_add_u32_e32 v0, 0x1400, v0
	v_lshl_add_u64 v[4:5], v[2:3], 0, v[4:5]
	v_lshlrev_b64 v[6:7], 10, v[6:7]
	v_ashrrev_i32_e32 v0, 6, v0
	v_lshl_add_u64 v[6:7], v[2:3], 0, v[6:7]
	global_load_dwordx4 v[98:101], v[4:5], off
	global_load_dwordx4 v[102:105], v[6:7], off
	v_max_i32_e32 v4, s8, v0
	v_min_i32_e32 v0, 0x17f, v8
	v_add_u32_e32 v0, 0x1600, v0
	v_ashrrev_i32_e32 v0, 6, v0
	v_ashrrev_i32_e32 v5, 31, v4
	v_max_i32_e32 v6, s8, v0
	v_lshl_add_u64 v[4:5], s[6:7], 0, v[4:5]
	v_ashrrev_i32_e32 v7, 31, v6
	v_lshlrev_b64 v[4:5], 10, v[4:5]
	v_lshl_add_u64 v[6:7], s[6:7], 0, v[6:7]
	v_lshl_add_u64 v[4:5], v[2:3], 0, v[4:5]
	v_lshlrev_b64 v[6:7], 10, v[6:7]
	v_lshl_add_u64 v[2:3], v[2:3], 0, v[6:7]
	global_load_dwordx4 v[106:109], v[4:5], off
	global_load_dwordx4 v[110:113], v[2:3], off
